# ret_kv unit: the four serial K-chunk staging loads (load, wait, ds_write x8) put in flight together with counted waits
# speedup vs baseline: 1.0031x; 1.0031x over previous
.LBB0_381:
	s_or_b64 exec, exec, s[8:9]
	v_mov_b32_e32 v1, s2
	s_waitcnt lgkmcnt(0)
	s_barrier
	ds_read_b32 v1, v1
	s_movk_i32 s3, 0x1ff
	s_mov_b64 s[10:11], -1
	s_waitcnt lgkmcnt(0)
	v_cmp_lt_i32_e32 vcc, s3, v1
	v_readfirstlane_b32 s8, v1
	s_cbranch_vccnz .LBB0_378
	v_mov_b32_e32 v1, v0
	s_mov_b32 s3, s88
	v_readlane_b32 s9, v252, 0
	s_lshl_b32 s3, s8, 5
	s_and_b32 s9, s3, 0xfffff000
	s_lshl_b32 s3, s8, 7
	s_bfe_u32 s16, s8, 0x20005
	s_and_b32 s3, s3, 0xf80
	s_mov_b64 s[10:11], s[68:69]
	s_or_b32 s9, s9, s3
	v_cvt_f32_ubyte0_e32 v2, s16
	s_add_u32 s14, s10, 0x9000000
	v_sub_f32_e32 v34, 0xc0a00000, v2
	s_mov_b32 s6, 0xc2fc0000
	s_addc_u32 s15, s11, 0
	v_cmp_gt_f32_e32 vcc, s6, v34
	v_ashrrev_i32_e32 v11, 4, v1
	v_readlane_b32 s28, v253, 17
	s_and_b64 s[12:13], vcc, exec
	v_lshlrev_b32_e32 v12, 3, v1
	v_add_u32_e32 v2, s9, v11
	v_mov_b64_e32 v[4:5], s[14:15]
	v_readlane_b32 s29, v253, 18
	s_cselect_b32 s12, 0xffffffc0, 0
	v_and_b32_e32 v10, 0x78, v12
	v_mad_i64_i32 v[6:7], s[14:15], v2, s24, v[4:5]
	s_mov_b32 s17, s29
	s_lshl_b32 s16, s16, 8
	v_lshl_add_u64 v[6:7], v[6:7], 0, s[16:17]
	v_lshlrev_b32_e32 v2, 1, v10
	v_lshl_add_u64 v[6:7], v[6:7], 0, v[2:3]
	s_barrier
	global_load_dwordx4 v[6:9], v[6:7], off offset:2048
	v_add_u32_e32 v37, 0x200, v1
	v_mov_b32_e32 v36, s72
	v_ashrrev_i32_e32 v13, 4, v37
	v_mad_u32_u24 v14, v10, s20, v36
	v_add_u32_e32 v10, s9, v13
	v_lshl_add_u32 v15, v11, 1, v14
	v_mad_i64_i32 v[10:11], s[14:15], v10, s24, v[4:5]
	v_lshl_add_u64 v[10:11], v[10:11], 0, s[16:17]
	v_lshl_add_u64 v[10:11], v[10:11], 0, v[2:3]
	v_lshl_add_u32 v13, v13, 1, v14
	global_load_dwordx4 v[66:69], v[10:11], off offset:2048
	v_add_u32_e32 v10, 0x400, v1
	v_ashrrev_i32_e32 v78, 4, v10
	v_add_u32_e32 v10, s9, v78
	v_mad_i64_i32 v[10:11], s[14:15], v10, s24, v[4:5]
	v_lshl_add_u64 v[10:11], v[10:11], 0, s[16:17]
	v_lshl_add_u64 v[10:11], v[10:11], 0, v[2:3]
	v_lshl_add_u32 v78, v78, 1, v14
	global_load_dwordx4 v[70:73], v[10:11], off offset:2048
	v_add_u32_e32 v10, 0x600, v1
	v_ashrrev_i32_e32 v79, 4, v10
	v_add_u32_e32 v10, s9, v79
	v_mad_i64_i32 v[10:11], s[14:15], v10, s24, v[4:5]
	v_lshl_add_u64 v[10:11], v[10:11], 0, s[16:17]
	v_lshl_add_u64 v[10:11], v[10:11], 0, v[2:3]
	v_lshl_add_u32 v80, v79, 1, v14
	global_load_dwordx4 v[74:77], v[10:11], off offset:2048
	v_ashrrev_i32_e32 v38, 3, v1
	v_and_b32_e32 v39, 56, v12
	v_mov_b32_e32 v55, 0x42800000
	v_cndmask_b32_e32 v35, 0, v55, vcc
	v_add_f32_e32 v34, v34, v35
	v_exp_f32_e32 v34, v34
	v_ashrrev_i32_e32 v37, 3, v37
	v_mad_u32_u24 v36, v39, s20, v36
	v_sub_u32_e32 v40, 0x7f, v38
	v_ldexp_f32 v34, v34, s12
	v_sub_f32_e32 v34, 1.0, v34
	v_cmp_gt_f32_e32 vcc, s25, v34
	s_and_b64 s[12:13], vcc, exec
	v_cvt_f32_i32_e32 v35, v40
	v_mov_b32_e32 v40, 0x42000000
	v_cndmask_b32_e32 v40, 0, v40, vcc
	v_not_b32_e32 v56, 63
	v_and_b32_e32 v54, 31, v1
	v_readlane_b32 s30, v253, 19
	v_readlane_b32 s31, v253, 20
	s_movk_i32 s7, 0x1000
	s_waitcnt vmcnt(3) lgkmcnt(0)
	ds_write_b16 v15, v6
	ds_write_b16_d16_hi v15, v6 offset:272
	ds_write_b16 v15, v7 offset:544
	ds_write_b16_d16_hi v15, v7 offset:816
	ds_write_b16 v15, v8 offset:1088
	ds_write_b16_d16_hi v15, v8 offset:1360
	ds_write_b16 v15, v9 offset:1632
	ds_write_b16_d16_hi v15, v9 offset:1904
	s_waitcnt vmcnt(2) lgkmcnt(0)
	ds_write_b16 v13, v66
	ds_write_b16_d16_hi v13, v66 offset:272
	ds_write_b16 v13, v67 offset:544
	ds_write_b16_d16_hi v13, v67 offset:816
	ds_write_b16 v13, v68 offset:1088
	ds_write_b16_d16_hi v13, v68 offset:1360
	ds_write_b16 v13, v69 offset:1632
	ds_write_b16_d16_hi v13, v69 offset:1904
	v_add_u32_e32 v2, s9, v38
	s_waitcnt vmcnt(1) lgkmcnt(0)
	ds_write_b16 v78, v70
	ds_write_b16_d16_hi v78, v70 offset:272
	ds_write_b16 v78, v71 offset:544
	ds_write_b16_d16_hi v78, v71 offset:816
	ds_write_b16 v78, v72 offset:1088
	ds_write_b16_d16_hi v78, v72 offset:1360
	ds_write_b16 v78, v73 offset:1632
	ds_write_b16_d16_hi v78, v73 offset:1904
	v_mad_i64_i32 v[10:11], s[14:15], v2, s24, v[4:5]
	v_lshlrev_b32_e32 v2, 2, v39
	v_lshl_add_u64 v[10:11], v[10:11], 0, s[16:17]
	v_lshl_add_u64 v[26:27], s[10:11], 0, v[2:3]
	v_lshlrev_b32_e32 v2, 1, v39
	s_mov_b64 s[14:15], 0x200000
	v_lshl_add_u64 v[14:15], v[10:11], 0, v[2:3]
	v_add_u32_e32 v39, s9, v37
	s_cselect_b32 s9, 32, 0
	v_ldexp_f32 v34, v34, s9
	v_log_f32_e32 v34, v34
	v_mad_i64_i32 v[4:5], s[12:13], v39, s24, v[4:5]
	v_lshl_add_u64 v[4:5], v[4:5], 0, s[16:17]
	v_sub_f32_e32 v34, v34, v40
	v_mul_f32_e32 v39, v34, v35
	v_cmp_gt_f32_e32 vcc, s6, v39
	v_lshl_add_u64 v[4:5], v[4:5], 0, v[2:3]
	s_mov_b32 s9, s29
	v_cndmask_b32_e32 v39, 0, v55, vcc
	v_fmac_f32_e32 v39, v34, v35
	v_exp_f32_e32 v35, v39
	v_cndmask_b32_e32 v2, 0, v56, vcc
	v_writelane_b32 v253, s8, 17
	s_waitcnt vmcnt(0) lgkmcnt(0)
	ds_write_b16 v80, v74
	ds_write_b16_d16_hi v80, v74 offset:272
	ds_write_b16 v80, v75 offset:544
	ds_write_b16_d16_hi v80, v75 offset:816
	ds_write_b16 v80, v76 offset:1088
	ds_write_b16_d16_hi v80, v76 offset:1360
	ds_write_b16 v80, v77 offset:1632
	ds_write_b16_d16_hi v80, v77 offset:1904
	v_add_lshl_u32 v6, v38, s3, 6
	v_ashrrev_i32_e32 v7, 31, v6
	v_lshlrev_b64 v[28:29], 2, v[6:7]
	v_lshl_add_u64 v[6:7], v[26:27], 0, s[14:15]
	global_load_dwordx4 v[10:13], v[14:15], off offset:1024
	s_nop 0
	global_load_dwordx4 v[14:17], v[14:15], off offset:1152
	v_lshl_add_u64 v[8:9], v[6:7], 0, v[28:29]
	s_mov_b64 s[14:15], 0x100000
	global_load_dwordx4 v[18:21], v[8:9], off
	global_load_dwordx4 v[22:25], v[8:9], off offset:16
	v_lshl_add_u64 v[8:9], v[26:27], 0, s[14:15]
	v_lshl_add_u64 v[30:31], v[8:9], 0, v[28:29]
	global_load_dwordx4 v[26:29], v[30:31], off
	s_nop 0
	global_load_dwordx4 v[30:33], v[30:31], off offset:16
	v_ldexp_f32 v2, v35, v2
	v_mul_f32_e32 v2, 0x3db504f3, v2
	v_lshl_add_u32 v38, v38, 1, v36
	v_writelane_b32 v253, s9, 18
	v_writelane_b32 v253, s10, 19
	v_writelane_b32 v253, s11, 20
	s_ashr_i32 s9, s8, 31
	s_lshl_b64 s[8:9], s[8:9], 16
	s_waitcnt vmcnt(0) lgkmcnt(0)
	v_lshlrev_b32_e32 v35, 16, v10
	v_lshlrev_b32_e32 v39, 16, v14
	v_and_b32_e32 v10, 0xffff0000, v10
	v_and_b32_e32 v14, 0xffff0000, v14
	v_lshlrev_b32_e32 v40, 16, v11
	v_and_b32_e32 v11, 0xffff0000, v11
	v_lshlrev_b32_e32 v41, 16, v15
	v_and_b32_e32 v15, 0xffff0000, v15
	v_lshlrev_b32_e32 v42, 16, v12
	v_and_b32_e32 v12, 0xffff0000, v12
	v_lshlrev_b32_e32 v43, 16, v16
	v_and_b32_e32 v16, 0xffff0000, v16
	v_lshlrev_b32_e32 v44, 16, v13
	v_and_b32_e32 v13, 0xffff0000, v13
	v_lshlrev_b32_e32 v45, 16, v17
	v_and_b32_e32 v17, 0xffff0000, v17
	v_mul_f32_e32 v46, v18, v39
	v_mul_f32_e32 v47, v19, v14
	v_mul_f32_e32 v18, v18, v35
	v_mul_f32_e32 v19, v19, v10
	v_mul_f32_e32 v48, v20, v41
	v_mul_f32_e32 v49, v21, v15
	v_mul_f32_e32 v20, v20, v40
	v_mul_f32_e32 v21, v21, v11
	v_mul_f32_e32 v50, v22, v43
	v_mul_f32_e32 v51, v23, v16
	v_mul_f32_e32 v22, v22, v42
	v_mul_f32_e32 v23, v23, v12
	v_mul_f32_e32 v52, v24, v45
	v_mul_f32_e32 v53, v25, v17
	v_mul_f32_e32 v24, v24, v44
	v_mul_f32_e32 v25, v25, v13
	v_fma_f32 v35, v26, v35, -v46
	v_fma_f32 v10, v27, v10, -v47
	v_fmac_f32_e32 v18, v26, v39
	v_fmac_f32_e32 v19, v27, v14
	v_fma_f32 v14, v28, v40, -v48
	v_fma_f32 v11, v29, v11, -v49
	v_fmac_f32_e32 v20, v28, v41
	v_fmac_f32_e32 v21, v29, v15
	v_fma_f32 v15, v30, v42, -v50
	v_fma_f32 v12, v31, v12, -v51
	v_fmac_f32_e32 v22, v30, v43
	v_fmac_f32_e32 v23, v31, v16
	v_fma_f32 v16, v32, v44, -v52
	v_fma_f32 v13, v33, v13, -v53
	v_fmac_f32_e32 v24, v32, v45
	v_fmac_f32_e32 v25, v33, v17
	v_mul_f32_e32 v17, v2, v35
	v_mul_f32_e32 v10, v2, v10
	v_mul_f32_e32 v18, v2, v18
	v_mul_f32_e32 v19, v2, v19
	v_mul_f32_e32 v14, v2, v14
	v_mul_f32_e32 v11, v2, v11
	v_mul_f32_e32 v20, v2, v20
	v_mul_f32_e32 v21, v2, v21
	v_mul_f32_e32 v15, v2, v15
	v_mul_f32_e32 v12, v2, v12
	v_mul_f32_e32 v22, v2, v22
	v_mul_f32_e32 v23, v2, v23
	v_mul_f32_e32 v16, v2, v16
	v_mul_f32_e32 v13, v2, v13
	v_mul_f32_e32 v24, v2, v24
	v_mul_f32_e32 v2, v2, v25
	v_cvt_pk_bf16_f32 v17, v17, s0
	v_cvt_pk_bf16_f32 v10, v10, s0
	v_cvt_pk_bf16_f32 v18, v18, s0
	v_cvt_pk_bf16_f32 v19, v19, s0
	v_cvt_pk_bf16_f32 v14, v14, s0
	v_cvt_pk_bf16_f32 v11, v11, s0
	v_cvt_pk_bf16_f32 v20, v20, s0
	v_cvt_pk_bf16_f32 v21, v21, s0
	v_cvt_pk_bf16_f32 v15, v15, s0
	v_cvt_pk_bf16_f32 v12, v12, s0
	v_cvt_pk_bf16_f32 v22, v22, s0
	v_cvt_pk_bf16_f32 v23, v23, s0
	v_cvt_pk_bf16_f32 v16, v16, s0
	v_cvt_pk_bf16_f32 v13, v13, s0
	v_cvt_pk_bf16_f32 v24, v24, s0
	v_cvt_pk_bf16_f32 v2, v2, s0
	ds_write_b16 v38, v17 offset:34816
	ds_write_b16 v38, v10 offset:35088
	ds_write_b16 v38, v18 offset:52224
	ds_write_b16 v38, v19 offset:52496
	ds_write_b16 v38, v14 offset:35360
	ds_write_b16 v38, v11 offset:35632
	ds_write_b16 v38, v20 offset:52768
	ds_write_b16 v38, v21 offset:53040
	ds_write_b16 v38, v15 offset:35904
	ds_write_b16 v38, v12 offset:36176
	ds_write_b16 v38, v22 offset:53312
	ds_write_b16 v38, v23 offset:53584
	ds_write_b16 v38, v16 offset:36448
	ds_write_b16 v38, v13 offset:36720
	ds_write_b16 v38, v24 offset:53856
	ds_write_b16 v38, v2 offset:54128
	global_load_dwordx4 v[10:13], v[4:5], off offset:1024
	global_load_dwordx4 v[14:17], v[4:5], off offset:1152
	v_add_lshl_u32 v4, v37, s3, 6
	v_ashrrev_i32_e32 v5, 31, v4
	v_lshlrev_b64 v[22:23], 2, v[4:5]
	v_lshl_add_u64 v[18:19], v[6:7], 0, v[22:23]
	global_load_dwordx4 v[4:7], v[18:19], off
	s_nop 0
	global_load_dwordx4 v[18:21], v[18:19], off offset:16
	v_lshl_add_u64 v[8:9], v[8:9], 0, v[22:23]
	global_load_dwordx4 v[22:25], v[8:9], off
	global_load_dwordx4 v[26:29], v[8:9], off offset:16
	v_sub_u32_e32 v8, 0x7f, v37
	v_cvt_f32_i32_e32 v8, v8
	v_readfirstlane_b32 s3, v1
	v_bfe_u32 v1, v1, 5, 1
	s_ashr_i32 s14, s3, 7
	v_lshl_add_u32 v2, v1, 4, s72
	v_lshl_or_b32 v30, s14, 5, v54
	v_mad_u64_u32 v[52:53], s[12:13], v30, s20, v[2:3]
	v_mul_f32_e32 v30, v34, v8
	v_cmp_gt_f32_e32 vcc, s6, v30
	v_lshl_add_u32 v9, v37, 1, v36
	s_add_u32 s8, s10, s8
	v_cndmask_b32_e32 v30, 0, v55, vcc
	v_fmac_f32_e32 v30, v34, v8
	v_exp_f32_e32 v8, v30
	v_cndmask_b32_e32 v30, 0, v56, vcc
	s_addc_u32 s9, s11, s9
	s_add_u32 s8, s8, 0x4b900000
	v_ldexp_f32 v8, v8, v30
	v_mul_f32_e32 v8, 0x3db504f3, v8
	s_addc_u32 s9, s9, 0
	s_and_b32 s3, s3, 64
	v_or_b32_e32 v53, s3, v54
	v_mad_u32_u24 v56, v53, s20, v2
	v_lshlrev_b32_e32 v1, 9, v1
	s_lshl_b32 s10, s14, 12
	v_or3_b32 v1, s10, v1, v54
	v_or_b32_e32 v60, s3, v1
	v_ashrrev_i32_e32 v61, 31, v60
	v_lshl_add_u64 v[62:63], v[60:61], 2, s[8:9]
	v_add_co_u32_e32 v64, vcc, s7, v62
	s_movk_i32 s3, 0x2000
	s_nop 0
	v_addc_co_u32_e32 v65, vcc, 0, v63, vcc
	s_movk_i32 s6, 0x3000
	v_ashrrev_i32_e32 v61, 31, v1
	s_mov_b64 s[10:11], 0
	s_waitcnt vmcnt(0) lgkmcnt(0)
	v_and_b32_e32 v37, 0xffff0000, v13
	v_lshlrev_b32_e32 v31, 16, v14
	v_and_b32_e32 v36, 0xffff0000, v17
	v_lshlrev_b32_e32 v17, 16, v17
	v_lshlrev_b32_e32 v13, 16, v13
	v_lshlrev_b32_e32 v30, 16, v10
	v_and_b32_e32 v10, 0xffff0000, v10
	v_and_b32_e32 v14, 0xffff0000, v14
	v_lshlrev_b32_e32 v32, 16, v11
	v_and_b32_e32 v11, 0xffff0000, v11
	v_lshlrev_b32_e32 v33, 16, v15
	v_and_b32_e32 v15, 0xffff0000, v15
	v_lshlrev_b32_e32 v34, 16, v12
	v_and_b32_e32 v12, 0xffff0000, v12
	v_lshlrev_b32_e32 v35, 16, v16
	v_and_b32_e32 v16, 0xffff0000, v16
	v_mul_f32_e32 v38, v4, v31
	v_mul_f32_e32 v44, v20, v17
	v_mul_f32_e32 v20, v20, v13
	v_mul_f32_e32 v39, v5, v14
	v_mul_f32_e32 v4, v4, v30
	v_mul_f32_e32 v5, v5, v10
	v_mul_f32_e32 v40, v6, v33
	v_mul_f32_e32 v41, v7, v15
	v_mul_f32_e32 v6, v6, v32
	v_mul_f32_e32 v7, v7, v11
	v_mul_f32_e32 v42, v18, v35
	v_mul_f32_e32 v43, v19, v16
	v_mul_f32_e32 v18, v18, v34
	v_mul_f32_e32 v19, v19, v12
	v_mul_f32_e32 v45, v21, v36
	v_mul_f32_e32 v21, v21, v37
	v_fma_f32 v30, v22, v30, -v38
	v_fmac_f32_e32 v20, v28, v17
	v_fma_f32 v10, v23, v10, -v39
	v_fmac_f32_e32 v4, v22, v31
	v_fmac_f32_e32 v5, v23, v14
	v_fma_f32 v14, v24, v32, -v40
	v_fma_f32 v11, v25, v11, -v41
	v_fmac_f32_e32 v6, v24, v33
	v_fmac_f32_e32 v7, v25, v15
	v_fma_f32 v15, v26, v34, -v42
	v_fma_f32 v12, v27, v12, -v43
	v_fmac_f32_e32 v18, v26, v35
	v_fmac_f32_e32 v19, v27, v16
	v_fma_f32 v13, v28, v13, -v44
	v_fma_f32 v16, v29, v37, -v45
	v_fmac_f32_e32 v21, v29, v36
	v_mul_f32_e32 v17, v8, v30
	v_mul_f32_e32 v20, v8, v20
	v_mul_f32_e32 v10, v8, v10
	v_mul_f32_e32 v4, v8, v4
	v_mul_f32_e32 v5, v8, v5
	v_mul_f32_e32 v14, v8, v14
	v_mul_f32_e32 v11, v8, v11
	v_mul_f32_e32 v6, v8, v6
	v_mul_f32_e32 v7, v8, v7
	v_mul_f32_e32 v15, v8, v15
	v_mul_f32_e32 v12, v8, v12
	v_mul_f32_e32 v18, v8, v18
	v_mul_f32_e32 v19, v8, v19
	v_mul_f32_e32 v13, v8, v13
	v_mul_f32_e32 v16, v8, v16
	v_mul_f32_e32 v8, v8, v21
	v_cvt_pk_bf16_f32 v17, v17, s0
	v_cvt_pk_bf16_f32 v20, v20, s0
	v_cvt_pk_bf16_f32 v10, v10, s0
	v_cvt_pk_bf16_f32 v4, v4, s0
	v_cvt_pk_bf16_f32 v5, v5, s0
	v_cvt_pk_bf16_f32 v14, v14, s0
	v_cvt_pk_bf16_f32 v11, v11, s0
	v_cvt_pk_bf16_f32 v6, v6, s0
	v_cvt_pk_bf16_f32 v7, v7, s0
	v_cvt_pk_bf16_f32 v15, v15, s0
	v_cvt_pk_bf16_f32 v12, v12, s0
	v_cvt_pk_bf16_f32 v18, v18, s0
	v_cvt_pk_bf16_f32 v19, v19, s0
	v_cvt_pk_bf16_f32 v13, v13, s0
	v_cvt_pk_bf16_f32 v16, v16, s0
	v_cvt_pk_bf16_f32 v8, v8, s0
	ds_write_b16 v9, v17 offset:34816
	ds_write_b16 v9, v10 offset:35088
	ds_write_b16 v9, v4 offset:52224
	ds_write_b16 v9, v5 offset:52496
	ds_write_b16 v9, v14 offset:35360
	ds_write_b16 v9, v11 offset:35632
	ds_write_b16 v9, v6 offset:52768
	ds_write_b16 v9, v7 offset:53040
	ds_write_b16 v9, v15 offset:35904
	ds_write_b16 v9, v12 offset:36176
	ds_write_b16 v9, v18 offset:53312
	ds_write_b16 v9, v19 offset:53584
	ds_write_b16 v9, v13 offset:36448
	ds_write_b16 v9, v16 offset:36720
	ds_write_b16 v9, v20 offset:53856
	ds_write_b16 v9, v8 offset:54128
	s_waitcnt lgkmcnt(0)
	s_barrier
	ds_read_b128 v[20:23], v52
	ds_read_b128 v[4:7], v56 offset:34816
	ds_read_b128 v[24:27], v52 offset:32
	ds_read_b128 v[28:31], v56 offset:34848
	s_waitcnt lgkmcnt(2)
	v_mfma_f32_32x32x16_bf16 v[4:19], v[20:23], v[4:7], 0
	s_waitcnt lgkmcnt(0)
	v_mfma_f32_32x32x16_bf16 v[4:19], v[24:27], v[28:31], v[4:19]
	ds_read_b128 v[28:31], v52 offset:64
	ds_read_b128 v[32:35], v56 offset:34880
	ds_read_b128 v[36:39], v52 offset:96
	ds_read_b128 v[40:43], v56 offset:34912
	s_waitcnt lgkmcnt(2)
	v_mfma_f32_32x32x16_bf16 v[4:19], v[28:31], v[32:35], v[4:19]
	s_waitcnt lgkmcnt(0)
	v_mfma_f32_32x32x16_bf16 v[4:19], v[36:39], v[40:43], v[4:19]
	ds_read_b128 v[32:35], v52 offset:128
	ds_read_b128 v[40:43], v56 offset:34944
	ds_read_b128 v[44:47], v52 offset:160
	ds_read_b128 v[48:51], v56 offset:34976
	s_waitcnt lgkmcnt(2)
	v_mfma_f32_32x32x16_bf16 v[4:19], v[32:35], v[40:43], v[4:19]
	v_or_b32_e32 v40, 32, v53
	v_mad_u32_u24 v2, v40, s20, v2
	ds_read_b128 v[40:43], v52 offset:192
	s_waitcnt lgkmcnt(1)
	v_mfma_f32_32x32x16_bf16 v[4:19], v[44:47], v[48:51], v[4:19]
	ds_read_b128 v[48:51], v56 offset:35008
	ds_read_b128 v[52:55], v52 offset:224
	ds_read_b128 v[56:59], v56 offset:35040
	s_waitcnt lgkmcnt(2)
	v_mfma_f32_32x32x16_bf16 v[4:19], v[40:43], v[48:51], v[4:19]
	v_add_co_u32_e32 v48, vcc, s3, v62
	s_nop 1
	v_addc_co_u32_e32 v49, vcc, 0, v63, vcc
	v_add_co_u32_e32 v50, vcc, s6, v62
	s_waitcnt lgkmcnt(0)
	v_mfma_f32_32x32x16_bf16 v[4:19], v[52:55], v[56:59], v[4:19]
	v_addc_co_u32_e32 v51, vcc, 0, v63, vcc
	s_nop 10
	global_store_dword v[62:63], v4, off
	global_store_dword v[62:63], v5, off offset:512
	global_store_dword v[62:63], v6, off offset:1024
	global_store_dword v[62:63], v7, off offset:1536
	global_store_dword v[64:65], v8, off
	global_store_dword v[64:65], v9, off offset:512
	global_store_dword v[64:65], v10, off offset:1024
	global_store_dword v[64:65], v11, off offset:1536
	global_store_dword v[48:49], v12, off
	global_store_dword v[48:49], v13, off offset:512
	global_store_dword v[48:49], v14, off offset:1024
	global_store_dword v[48:49], v15, off offset:1536
	global_store_dword v[50:51], v16, off
	global_store_dword v[50:51], v17, off offset:512
	global_store_dword v[50:51], v18, off offset:1024
	global_store_dword v[50:51], v19, off offset:1536
	ds_read_b128 v[4:7], v2 offset:34816
	ds_read_b128 v[48:51], v2 offset:34848
	s_waitcnt lgkmcnt(0)
	v_mfma_f32_32x32x16_bf16 v[4:19], v[20:23], v[4:7], 0
	v_mfma_f32_32x32x16_bf16 v[4:19], v[24:27], v[48:51], v[4:19]
	ds_read_b128 v[20:23], v2 offset:34880
	ds_read_b128 v[24:27], v2 offset:34912
	s_waitcnt lgkmcnt(0)
	v_mfma_f32_32x32x16_bf16 v[4:19], v[28:31], v[20:23], v[4:19]
	v_lshl_add_u64 v[28:29], v[60:61], 2, s[8:9]
	v_add_co_u32_e32 v30, vcc, s7, v28
	s_nop 1
	v_addc_co_u32_e32 v31, vcc, 0, v29, vcc
	v_mfma_f32_32x32x16_bf16 v[4:19], v[36:39], v[24:27], v[4:19]
	ds_read_b128 v[20:23], v2 offset:34944
	ds_read_b128 v[24:27], v2 offset:34976
	s_waitcnt lgkmcnt(0)
	v_mfma_f32_32x32x16_bf16 v[4:19], v[32:35], v[20:23], v[4:19]
	ds_read_b128 v[20:23], v2 offset:35008
	v_add_co_u32_e32 v32, vcc, s3, v28
	s_nop 1
	v_addc_co_u32_e32 v33, vcc, 0, v29, vcc
	v_mfma_f32_32x32x16_bf16 v[4:19], v[44:47], v[24:27], v[4:19]
	ds_read_b128 v[24:27], v2 offset:35040
	s_waitcnt lgkmcnt(0)
	v_mfma_f32_32x32x16_bf16 v[4:19], v[40:43], v[20:23], v[4:19]
	v_add_co_u32_e32 v20, vcc, 0x3000, v28
	s_nop 1
	v_addc_co_u32_e32 v21, vcc, 0, v29, vcc
	v_mfma_f32_32x32x16_bf16 v[4:19], v[52:55], v[24:27], v[4:19]
	s_nop 11
	global_store_dword v[28:29], v4, off offset:128
	global_store_dword v[28:29], v5, off offset:640
	global_store_dword v[28:29], v6, off offset:1152
	global_store_dword v[28:29], v7, off offset:1664
	global_store_dword v[30:31], v8, off offset:128
	global_store_dword v[30:31], v9, off offset:640
	global_store_dword v[30:31], v10, off offset:1152
	global_store_dword v[30:31], v11, off offset:1664
	global_store_dword v[32:33], v12, off offset:128
	global_store_dword v[32:33], v13, off offset:640
	global_store_dword v[32:33], v14, off offset:1152
	global_store_dword v[32:33], v15, off offset:1664
	global_store_dword v[20:21], v16, off offset:128
	global_store_dword v[20:21], v17, off offset:640
	global_store_dword v[20:21], v18, off offset:1152
	global_store_dword v[20:21], v19, off offset:1664
	s_branch .LBB0_378
